# speedup vs baseline: 1.0071x; 1.0071x over previous
.LE_join25:
	v_mfma_f32_32x32x16_f16 v[16:31], a[192:195], v[164:167], v[16:31]
	ds_read_b128 v[164:167], v193 offset:41984
	v_mfma_f32_32x32x16_f16 v[0:15], a[196:199], v[168:171], v[0:15]
	ds_read_b128 v[168:171], v193 offset:43008
	v_mfma_f32_32x32x16_f16 v[16:31], a[196:199], v[172:175], v[16:31]
	ds_read_b128 v[172:175], v193 offset:44032
	global_load_lds_dwordx4 v192, s[44:45] offset:1024 sc1
	s_waitcnt lgkmcnt(4)
	v_mfma_f32_32x32x16_f16 v[0:15], a[200:203], v[176:179], v[0:15]
	ds_read_b128 v[176:179], v193 offset:45056
	s_and_b32 s64, s33, 1
	s_lshl_b32 s64, s64, 22
	s_add_u32 s64, s64, s50
	s_add_u32 s36, s6, s64
	s_addc_u32 s37, s7, 0
	s_lshl_b32 s64, s33, 3
	s_add_u32 s64, s64, s29
	s_lshl_b32 s64, s64, 5
	s_add_u32 s64, s64, s30
	s_lshl_b32 s64, s64, 2
	s_add_u32 s40, s8, s64
	s_addc_u32 s41, s9, 0
	s_lshl_b32 s64, s33, 11
	s_lshl_b32 s65, s29, 8
	s_add_u32 s64, s64, s65
	s_add_u32 s64, s64, 192
	s_lshl_b32 s64, s64, 3
	s_add_u32 s42, s12, s64
	s_addc_u32 s43, s13, 0
	v_mfma_f32_32x32x16_f16 v[16:31], a[200:203], v[180:183], v[16:31]
	ds_read_b128 v[180:183], v193 offset:46080
	v_mfma_f32_32x32x16_f16 v[0:15], a[204:207], v[184:187], v[0:15]
	ds_read_b128 v[184:187], v193 offset:47104
	v_mfma_f32_32x32x16_f16 v[16:31], a[204:207], v[188:191], v[16:31]
	ds_read_b128 v[188:191], v193 offset:48128
	global_load_lds_dwordx4 v192, s[44:45] offset:2048 sc1
	s_waitcnt lgkmcnt(4)
	v_mfma_f32_32x32x16_f16 v[0:15], a[208:211], v[160:163], v[0:15]
	ds_read_b128 v[160:163], v193 offset:49152
	v_mfma_f32_32x32x16_f16 v[16:31], a[208:211], v[164:167], v[16:31]
	ds_read_b128 v[164:167], v193 offset:50176
	v_mfma_f32_32x32x16_f16 v[0:15], a[212:215], v[168:171], v[0:15]
	ds_read_b128 v[168:171], v193 offset:51200
	v_mfma_f32_32x32x16_f16 v[16:31], a[212:215], v[172:175], v[16:31]
	ds_read_b128 v[172:175], v193 offset:52224
	global_load_lds_dwordx4 v192, s[44:45] offset:3072 sc1
	s_waitcnt lgkmcnt(4)
	v_mfma_f32_32x32x16_f16 v[0:15], a[216:219], v[176:179], v[0:15]
	ds_read_b128 v[176:179], v193 offset:53248
	v_mfma_f32_32x32x16_f16 v[16:31], a[216:219], v[180:183], v[16:31]
	ds_read_b128 v[180:183], v193 offset:54272
	v_mfma_f32_32x32x16_f16 v[0:15], a[220:223], v[184:187], v[0:15]
	ds_read_b128 v[184:187], v193 offset:55296
	v_mfma_f32_32x32x16_f16 v[16:31], a[220:223], v[188:191], v[16:31]
	ds_read_b128 v[188:191], v193 offset:56320
	s_add_u32 s44, s34, 0x9000
	s_addc_u32 s45, s35, 0
	s_mov_b32 m0, s55
	s_nop 0
	global_load_lds_dwordx4 v192, s[44:45] sc1
	s_waitcnt lgkmcnt(4)
	v_mfma_f32_32x32x16_f16 v[0:15], a[224:227], v[160:163], v[0:15]
	ds_read_b128 v[160:163], v193 offset:57344
	v_mfma_f32_32x32x16_f16 v[16:31], a[224:227], v[164:167], v[16:31]
	ds_read_b128 v[164:167], v193 offset:58368
	v_mfma_f32_32x32x16_f16 v[0:15], a[228:231], v[168:171], v[0:15]
	ds_read_b128 v[168:171], v193 offset:59392
	v_mfma_f32_32x32x16_f16 v[16:31], a[228:231], v[172:175], v[16:31]
	ds_read_b128 v[172:175], v193 offset:60416
	global_load_lds_dwordx4 v192, s[44:45] offset:1024 sc1
	s_waitcnt lgkmcnt(4)
	v_mfma_f32_32x32x16_f16 v[0:15], a[232:235], v[176:179], v[0:15]
	ds_read_b128 v[176:179], v193 offset:61440
	v_mfma_f32_32x32x16_f16 v[16:31], a[232:235], v[180:183], v[16:31]
	ds_read_b128 v[180:183], v193 offset:62464
	v_mfma_f32_32x32x16_f16 v[0:15], a[236:239], v[184:187], v[0:15]
	ds_read_b128 v[184:187], v193 offset:63488
	v_mfma_f32_32x32x16_f16 v[16:31], a[236:239], v[188:191], v[16:31]
	ds_read_b128 v[188:191], v193 offset:64512
	global_load_lds_dwordx4 v192, s[44:45] offset:2048 sc1
	s_waitcnt vmcnt(8)
	s_barrier
	s_waitcnt lgkmcnt(4)
	v_mfma_f32_32x32x16_f16 v[0:15], a[240:243], v[160:163], v[0:15]
	ds_read_b128 v[160:163], v192 offset:0
	v_mfma_f32_32x32x16_f16 v[16:31], a[240:243], v[164:167], v[16:31]
	ds_read_b128 v[164:167], v192 offset:1024
	v_mfma_f32_32x32x16_f16 v[0:15], a[244:247], v[168:171], v[0:15]
	ds_read_b128 v[168:171], v192 offset:2048
	v_mfma_f32_32x32x16_f16 v[16:31], a[244:247], v[172:175], v[16:31]
	ds_read_b128 v[172:175], v192 offset:3072
	global_load_lds_dwordx4 v192, s[44:45] offset:3072 sc1
	s_waitcnt lgkmcnt(4)
	v_mfma_f32_32x32x16_f16 v[0:15], a[248:251], v[176:179], v[0:15]
	ds_read_b128 v[176:179], v192 offset:4096
	v_mfma_f32_32x32x16_f16 v[16:31], a[248:251], v[180:183], v[16:31]
	ds_read_b128 v[180:183], v192 offset:5120
	v_mfma_f32_32x32x16_f16 v[0:15], a[252:255], v[184:187], v[0:15]
	ds_read_b128 v[184:187], v192 offset:6144
	v_mfma_f32_32x32x16_f16 v[16:31], a[252:255], v[188:191], v[16:31]
	ds_read_b128 v[188:191], v192 offset:7168
	s_add_u32 s44, s34, 0x10000
	s_addc_u32 s45, s35, 0
	s_mov_b32 m0, s56
	s_nop 0
	global_load_lds_dwordx4 v192, s[44:45] sc1
	s_nop 3
	global_load_dword v228, v249, s[42:43] offset:0
	global_load_dword v229, v249, s[42:43] offset:256
	s_waitcnt lgkmcnt(4)
	v_mfma_f32_32x32x16_f16 v[32:47], a[0:3], v[160:163], v[32:47]
	ds_read_b128 v[160:163], v192 offset:8192
	v_exp_f32_e32 v200, v0
	v_mfma_f32_32x32x16_f16 v[48:63], a[0:3], v[164:167], v[48:63]
	ds_read_b128 v[164:167], v192 offset:9216
	s_lshl_b32 s64, s71, 3
	s_add_u32 s64, s64, s29
	s_lshl_b32 s64, s64, 7
	s_add_u32 s38, s8, s64
	s_addc_u32 s39, s9, 0
	global_load_dword v251, v196, s[38:39] sc1
	v_exp_f32_e32 v201, v1
	v_add_f32_e32 v200, 1.0, v200
	v_mfma_f32_32x32x16_f16 v[32:47], a[4:7], v[168:171], v[32:47]
	ds_read_b128 v[168:171], v192 offset:10240
	v_exp_f32_e32 v202, v2
	v_add_f32_e32 v201, 1.0, v201
	v_mfma_f32_32x32x16_f16 v[48:63], a[4:7], v[172:175], v[48:63]
	ds_read_b128 v[172:175], v192 offset:11264
	global_load_lds_dwordx4 v192, s[44:45] offset:1024 sc1
	v_exp_f32_e32 v203, v3
	v_add_f32_e32 v202, 1.0, v202
	s_waitcnt lgkmcnt(4)
	v_mfma_f32_32x32x16_f16 v[32:47], a[8:11], v[176:179], v[32:47]
	ds_read_b128 v[176:179], v192 offset:12288
	v_exp_f32_e32 v204, v4
	v_add_f32_e32 v203, 1.0, v203
	v_mfma_f32_32x32x16_f16 v[48:63], a[8:11], v[180:183], v[48:63]
	ds_read_b128 v[180:183], v192 offset:13312
	v_exp_f32_e32 v205, v5
	v_add_f32_e32 v204, 1.0, v204
	v_mfma_f32_32x32x16_f16 v[32:47], a[12:15], v[184:187], v[32:47]
	ds_read_b128 v[184:187], v192 offset:14336
	v_exp_f32_e32 v206, v6
	v_add_f32_e32 v205, 1.0, v205
	v_mfma_f32_32x32x16_f16 v[48:63], a[12:15], v[188:191], v[48:63]
	ds_read_b128 v[188:191], v192 offset:15360
	global_load_lds_dwordx4 v192, s[44:45] offset:2048 sc1
	v_exp_f32_e32 v207, v7
	v_add_f32_e32 v206, 1.0, v206
	s_waitcnt lgkmcnt(4)
	v_mfma_f32_32x32x16_f16 v[32:47], a[16:19], v[160:163], v[32:47]
	ds_read_b128 v[160:163], v192 offset:16384
	v_exp_f32_e32 v208, v8
	v_add_f32_e32 v207, 1.0, v207
	v_mfma_f32_32x32x16_f16 v[48:63], a[16:19], v[164:167], v[48:63]
	ds_read_b128 v[164:167], v192 offset:17408
	v_exp_f32_e32 v209, v9
	v_add_f32_e32 v208, 1.0, v208
	v_mfma_f32_32x32x16_f16 v[32:47], a[20:23], v[168:171], v[32:47]
	ds_read_b128 v[168:171], v192 offset:18432
	v_exp_f32_e32 v210, v10
	v_add_f32_e32 v209, 1.0, v209
	v_mfma_f32_32x32x16_f16 v[48:63], a[20:23], v[172:175], v[48:63]
	ds_read_b128 v[172:175], v192 offset:19456
	global_load_lds_dwordx4 v192, s[44:45] offset:3072 sc1
	v_exp_f32_e32 v211, v11
	v_add_f32_e32 v210, 1.0, v210
	s_waitcnt lgkmcnt(4)
	v_mfma_f32_32x32x16_f16 v[32:47], a[24:27], v[176:179], v[32:47]
	ds_read_b128 v[176:179], v192 offset:20480
	v_exp_f32_e32 v212, v12
	v_add_f32_e32 v211, 1.0, v211
	v_mfma_f32_32x32x16_f16 v[48:63], a[24:27], v[180:183], v[48:63]
	ds_read_b128 v[180:183], v192 offset:21504
	v_exp_f32_e32 v213, v13
	v_add_f32_e32 v212, 1.0, v212
	v_mfma_f32_32x32x16_f16 v[32:47], a[28:31], v[184:187], v[32:47]
	ds_read_b128 v[184:187], v192 offset:22528
	v_exp_f32_e32 v214, v14
	v_add_f32_e32 v213, 1.0, v213
	v_mfma_f32_32x32x16_f16 v[48:63], a[28:31], v[188:191], v[48:63]
	ds_read_b128 v[188:191], v192 offset:23552
	s_add_u32 s44, s34, 0x11000
	s_addc_u32 s45, s35, 0
	s_mov_b32 m0, s57
	s_nop 0
	global_load_lds_dwordx4 v192, s[44:45] sc1
	v_exp_f32_e32 v215, v15
	v_add_f32_e32 v214, 1.0, v214
	s_waitcnt lgkmcnt(4)
	v_mfma_f32_32x32x16_f16 v[32:47], a[32:35], v[160:163], v[32:47]
	ds_read_b128 v[160:163], v192 offset:24576
	v_add_f32_e32 v215, 1.0, v215
	v_rcp_f32_e32 v200, v200
	v_mfma_f32_32x32x16_f16 v[48:63], a[32:35], v[164:167], v[48:63]
	ds_read_b128 v[164:167], v192 offset:25600
	v_rcp_f32_e32 v201, v201
	v_mfma_f32_32x32x16_f16 v[32:47], a[36:39], v[168:171], v[32:47]
	ds_read_b128 v[168:171], v192 offset:26624
	v_rcp_f32_e32 v202, v202
	v_mfma_f32_32x32x16_f16 v[48:63], a[36:39], v[172:175], v[48:63]
	ds_read_b128 v[172:175], v192 offset:27648
	global_load_lds_dwordx4 v192, s[44:45] offset:1024 sc1
	v_rcp_f32_e32 v203, v203
	s_waitcnt lgkmcnt(4)
	v_mfma_f32_32x32x16_f16 v[32:47], a[40:43], v[176:179], v[32:47]
	ds_read_b128 v[176:179], v192 offset:28672
	v_rcp_f32_e32 v204, v204
	v_mfma_f32_32x32x16_f16 v[48:63], a[40:43], v[180:183], v[48:63]
	ds_read_b128 v[180:183], v192 offset:29696
	v_rcp_f32_e32 v205, v205
	v_mul_f32_e32 v204, v204, v128
	v_mfma_f32_32x32x16_f16 v[32:47], a[44:47], v[184:187], v[32:47]
	ds_read_b128 v[184:187], v192 offset:30720
	v_rcp_f32_e32 v206, v206
	v_mul_f32_e32 v205, v205, v129
	v_mfma_f32_32x32x16_f16 v[48:63], a[44:47], v[188:191], v[48:63]
	ds_read_b128 v[188:191], v192 offset:31744
	global_load_lds_dwordx4 v192, s[44:45] offset:2048 sc1
	v_rcp_f32_e32 v207, v207
	v_mul_f32_e32 v206, v206, v130
	s_waitcnt vmcnt(10)
	s_barrier
	s_waitcnt lgkmcnt(4)
	v_mfma_f32_32x32x16_f16 v[32:47], a[48:51], v[160:163], v[32:47]
	ds_read_b128 v[160:163], v192 offset:32768
	v_rcp_f32_e32 v208, v208
	v_mul_f32_e32 v207, v207, v131
	v_mfma_f32_32x32x16_f16 v[48:63], a[48:51], v[164:167], v[48:63]
	ds_read_b128 v[164:167], v192 offset:33792
	v_rcp_f32_e32 v209, v209
	v_fmamk_f32 v208, v208, 0xc0b8aa3b, v198
	v_mfma_f32_32x32x16_f16 v[32:47], a[52:55], v[168:171], v[32:47]
	ds_read_b128 v[168:171], v192 offset:34816
	v_rcp_f32_e32 v210, v210
	v_fmamk_f32 v209, v209, 0xc0b8aa3b, v198
	v_fma_f32 v128, v200, v208, v204
	v_mfma_f32_32x32x16_f16 v[48:63], a[52:55], v[172:175], v[48:63]
	ds_read_b128 v[172:175], v192 offset:35840
	global_load_lds_dwordx4 v192, s[44:45] offset:3072 sc1
	v_rcp_f32_e32 v211, v211
	v_fmamk_f32 v210, v210, 0xc0b8aa3b, v198
	v_fma_f32 v129, v201, v209, v205
	s_waitcnt lgkmcnt(4)
	v_mfma_f32_32x32x16_f16 v[32:47], a[56:59], v[176:179], v[32:47]
	ds_read_b128 v[176:179], v192 offset:36864
	v_rcp_f32_e32 v212, v212
	v_fmamk_f32 v211, v211, 0xc0b8aa3b, v198
	v_fma_f32 v130, v202, v210, v206
	v_mfma_f32_32x32x16_f16 v[48:63], a[56:59], v[180:183], v[48:63]
	ds_read_b128 v[180:183], v192 offset:37888
	v_rcp_f32_e32 v213, v213
	v_fma_f32 v131, v203, v211, v207
	v_mfma_f32_32x32x16_f16 v[32:47], a[60:63], v[184:187], v[32:47]
	ds_read_b128 v[184:187], v192 offset:38912
	v_rcp_f32_e32 v214, v214
	v_mfma_f32_32x32x16_f16 v[48:63], a[60:63], v[188:191], v[48:63]
	ds_read_b128 v[188:191], v192 offset:39936
	s_add_u32 s44, s34, 0x18000
	s_addc_u32 s45, s35, 0
	s_mov_b32 m0, s58
	s_nop 0
	global_load_lds_dwordx4 v192, s[44:45] sc1
	v_rcp_f32_e32 v215, v215
	s_waitcnt lgkmcnt(4)
	v_mfma_f32_32x32x16_f16 v[32:47], a[64:67], v[160:163], v[32:47]
	ds_read_b128 v[160:163], v192 offset:40960
	v_exp_f32_e32 v200, v128
	v_mfma_f32_32x32x16_f16 v[48:63], a[64:67], v[164:167], v[48:63]
	ds_read_b128 v[164:167], v192 offset:41984
	v_exp_f32_e32 v201, v129
	v_add_f32_e32 v200, 1.0, v200
	v_mfma_f32_32x32x16_f16 v[32:47], a[68:71], v[168:171], v[32:47]
	ds_read_b128 v[168:171], v192 offset:43008
	v_exp_f32_e32 v202, v130
	v_add_f32_e32 v201, 1.0, v201
	v_mfma_f32_32x32x16_f16 v[48:63], a[68:71], v[172:175], v[48:63]
	ds_read_b128 v[172:175], v192 offset:44032
	global_load_lds_dwordx4 v192, s[44:45] offset:1024 sc1
	v_exp_f32_e32 v203, v131
	v_add_f32_e32 v202, 1.0, v202
	s_waitcnt lgkmcnt(4)
	v_mfma_f32_32x32x16_f16 v[32:47], a[72:75], v[176:179], v[32:47]
	ds_read_b128 v[176:179], v192 offset:45056
	v_add_f32_e32 v203, 1.0, v203
	v_rcp_f32_e32 v200, v200
	v_mfma_f32_32x32x16_f16 v[48:63], a[72:75], v[180:183], v[48:63]
	ds_read_b128 v[180:183], v192 offset:46080
	v_rcp_f32_e32 v201, v201
	v_fma_f32 v200, v200, 2.0, -1.0
	v_mfma_f32_32x32x16_f16 v[32:47], a[76:79], v[184:187], v[32:47]
	ds_read_b128 v[184:187], v192 offset:47104
	v_rcp_f32_e32 v202, v202
	v_fma_f32 v201, v201, 2.0, -1.0
	v_mul_f32_e32 v216, v212, v200
	v_mfma_f32_32x32x16_f16 v[48:63], a[76:79], v[188:191], v[48:63]
	ds_read_b128 v[188:191], v192 offset:48128
	global_load_lds_dwordx4 v192, s[44:45] offset:2048 sc1
	v_rcp_f32_e32 v203, v203
	v_fma_f32 v202, v202, 2.0, -1.0
	v_mul_f32_e32 v217, v213, v201
	s_waitcnt lgkmcnt(4)
	v_mfma_f32_32x32x16_f16 v[32:47], a[80:83], v[160:163], v[32:47]
	ds_read_b128 v[160:163], v192 offset:49152
	v_fma_f32 v203, v203, 2.0, -1.0
	v_mul_f32_e32 v218, v214, v202
	v_exp_f32_e32 v200, v16
	v_mfma_f32_32x32x16_f16 v[48:63], a[80:83], v[164:167], v[48:63]
	ds_read_b128 v[164:167], v192 offset:50176
	v_mul_f32_e32 v219, v215, v203
	v_cvt_pk_f16_f32 v220, v216, v217
	v_exp_f32_e32 v201, v17
	v_mfma_f32_32x32x16_f16 v[32:47], a[84:87], v[168:171], v[32:47]
	ds_read_b128 v[168:171], v192 offset:51200
	v_cvt_pk_f16_f32 v221, v218, v219
	v_exp_f32_e32 v202, v18
	v_add_f32_e32 v200, 1.0, v200
	v_mfma_f32_32x32x16_f16 v[48:63], a[84:87], v[172:175], v[48:63]
	ds_read_b128 v[172:175], v192 offset:52224
	global_load_lds_dwordx4 v192, s[44:45] offset:3072 sc1
	s_cmp_lg_u32 s33, s60
	s_cbranch_scc1 .LE_nht26
	s_add_u32 s46, s62, 0x0
	s_addc_u32 s47, s63, 0
	global_store_dwordx4 v250, v[216:219], s[46:47]
	s_waitcnt vmcnt(0)

.LE_join33:
	v_mfma_f32_32x32x16_f16 v[32:47], a[196:199], v[168:171], v[32:47]
	ds_read_b128 v[168:171], v193 offset:43008
	v_mfma_f32_32x32x16_f16 v[48:63], a[196:199], v[172:175], v[48:63]
	ds_read_b128 v[172:175], v193 offset:44032
	global_load_lds_dwordx4 v192, s[44:45] offset:1024 sc1
	s_waitcnt lgkmcnt(4)
	v_mfma_f32_32x32x16_f16 v[32:47], a[200:203], v[176:179], v[32:47]
	ds_read_b128 v[176:179], v193 offset:45056
	v_mfma_f32_32x32x16_f16 v[48:63], a[200:203], v[180:183], v[48:63]
	ds_read_b128 v[180:183], v193 offset:46080
	s_and_b32 s64, s33, 1
	s_lshl_b32 s64, s64, 22
	s_add_u32 s64, s64, s50
	s_add_u32 s64, s64, 0x20000
	s_add_u32 s36, s6, s64
	s_addc_u32 s37, s7, 0
	s_lshl_b32 s64, s33, 3
	s_add_u32 s64, s64, s29
	s_lshl_b32 s64, s64, 5
	s_add_u32 s64, s64, s30
	s_lshl_b32 s64, s64, 2
	s_add_u32 s40, s8, s64
	s_addc_u32 s41, s9, 0
	s_lshl_b32 s64, s61, 11
	s_lshl_b32 s65, s29, 8
	s_add_u32 s64, s64, s65
	s_lshl_b32 s64, s64, 3
	s_add_u32 s42, s12, s64
	s_addc_u32 s43, s13, 0
	v_mfma_f32_32x32x16_f16 v[32:47], a[204:207], v[184:187], v[32:47]
	ds_read_b128 v[184:187], v193 offset:47104
	v_mfma_f32_32x32x16_f16 v[48:63], a[204:207], v[188:191], v[48:63]
	ds_read_b128 v[188:191], v193 offset:48128
	global_load_lds_dwordx4 v192, s[44:45] offset:2048 sc1
	s_waitcnt lgkmcnt(4)
	v_mfma_f32_32x32x16_f16 v[32:47], a[208:211], v[160:163], v[32:47]
	ds_read_b128 v[160:163], v193 offset:49152
	v_mfma_f32_32x32x16_f16 v[48:63], a[208:211], v[164:167], v[48:63]
	ds_read_b128 v[164:167], v193 offset:50176
	v_mfma_f32_32x32x16_f16 v[32:47], a[212:215], v[168:171], v[32:47]
	ds_read_b128 v[168:171], v193 offset:51200
	v_mfma_f32_32x32x16_f16 v[48:63], a[212:215], v[172:175], v[48:63]
	ds_read_b128 v[172:175], v193 offset:52224
	global_load_lds_dwordx4 v192, s[44:45] offset:3072 sc1
	s_waitcnt lgkmcnt(4)
	v_mfma_f32_32x32x16_f16 v[32:47], a[216:219], v[176:179], v[32:47]
	ds_read_b128 v[176:179], v193 offset:53248
	v_mfma_f32_32x32x16_f16 v[48:63], a[216:219], v[180:183], v[48:63]
	ds_read_b128 v[180:183], v193 offset:54272
	v_mfma_f32_32x32x16_f16 v[32:47], a[220:223], v[184:187], v[32:47]
	ds_read_b128 v[184:187], v193 offset:55296
	v_mfma_f32_32x32x16_f16 v[48:63], a[220:223], v[188:191], v[48:63]
	ds_read_b128 v[188:191], v193 offset:56320
	s_add_u32 s44, s34, 0x9000
	s_addc_u32 s45, s35, 0
	s_mov_b32 m0, s55
	s_nop 0
	global_load_lds_dwordx4 v192, s[44:45] sc1
	s_waitcnt lgkmcnt(4)
	v_mfma_f32_32x32x16_f16 v[32:47], a[224:227], v[160:163], v[32:47]
	ds_read_b128 v[160:163], v193 offset:57344
	v_mfma_f32_32x32x16_f16 v[48:63], a[224:227], v[164:167], v[48:63]
	ds_read_b128 v[164:167], v193 offset:58368
	v_mfma_f32_32x32x16_f16 v[32:47], a[228:231], v[168:171], v[32:47]
	ds_read_b128 v[168:171], v193 offset:59392
	v_mfma_f32_32x32x16_f16 v[48:63], a[228:231], v[172:175], v[48:63]
	ds_read_b128 v[172:175], v193 offset:60416
	global_load_lds_dwordx4 v192, s[44:45] offset:1024 sc1
	s_waitcnt lgkmcnt(4)
	v_mfma_f32_32x32x16_f16 v[32:47], a[232:235], v[176:179], v[32:47]
	ds_read_b128 v[176:179], v193 offset:61440
	v_mfma_f32_32x32x16_f16 v[48:63], a[232:235], v[180:183], v[48:63]
	ds_read_b128 v[180:183], v193 offset:62464
	v_mfma_f32_32x32x16_f16 v[32:47], a[236:239], v[184:187], v[32:47]
	ds_read_b128 v[184:187], v193 offset:63488
	v_mfma_f32_32x32x16_f16 v[48:63], a[236:239], v[188:191], v[48:63]
	ds_read_b128 v[188:191], v193 offset:64512
	global_load_lds_dwordx4 v192, s[44:45] offset:2048 sc1
	s_waitcnt vmcnt(8)
	s_barrier
	s_waitcnt lgkmcnt(4)
	v_mfma_f32_32x32x16_f16 v[32:47], a[240:243], v[160:163], v[32:47]
	ds_read_b128 v[160:163], v192 offset:0
	v_mfma_f32_32x32x16_f16 v[48:63], a[240:243], v[164:167], v[48:63]
	ds_read_b128 v[164:167], v192 offset:1024
	v_mfma_f32_32x32x16_f16 v[32:47], a[244:247], v[168:171], v[32:47]
	ds_read_b128 v[168:171], v192 offset:2048
	v_mfma_f32_32x32x16_f16 v[48:63], a[244:247], v[172:175], v[48:63]
	ds_read_b128 v[172:175], v192 offset:3072
	global_load_lds_dwordx4 v192, s[44:45] offset:3072 sc1
	s_waitcnt lgkmcnt(4)
	v_mfma_f32_32x32x16_f16 v[32:47], a[248:251], v[176:179], v[32:47]
	ds_read_b128 v[176:179], v192 offset:4096
	v_mfma_f32_32x32x16_f16 v[48:63], a[248:251], v[180:183], v[48:63]
	ds_read_b128 v[180:183], v192 offset:5120
	v_mfma_f32_32x32x16_f16 v[32:47], a[252:255], v[184:187], v[32:47]
	ds_read_b128 v[184:187], v192 offset:6144
	v_mfma_f32_32x32x16_f16 v[48:63], a[252:255], v[188:191], v[48:63]
	ds_read_b128 v[188:191], v192 offset:7168
	s_add_u32 s44, s34, 0x10000
	s_addc_u32 s45, s35, 0
	s_mov_b32 m0, s56
	s_nop 0
	global_load_lds_dwordx4 v192, s[44:45] sc1
	s_nop 3
	global_load_dword v228, v249, s[42:43] offset:0
	global_load_dword v229, v249, s[42:43] offset:256
	s_waitcnt lgkmcnt(4)
	v_mfma_f32_32x32x16_f16 v[64:79], a[0:3], v[160:163], v[64:79]
	ds_read_b128 v[160:163], v192 offset:8192
	v_exp_f32_e32 v200, v32
	v_mfma_f32_32x32x16_f16 v[80:95], a[0:3], v[164:167], v[80:95]
	ds_read_b128 v[164:167], v192 offset:9216
	s_lshl_b32 s64, s71, 3
	s_add_u32 s64, s64, s29
	s_lshl_b32 s64, s64, 7
	s_add_u32 s38, s8, s64
	s_addc_u32 s39, s9, 0
	global_load_dword v251, v196, s[38:39] sc1
	v_exp_f32_e32 v201, v33
	v_add_f32_e32 v200, 1.0, v200
	v_mfma_f32_32x32x16_f16 v[64:79], a[4:7], v[168:171], v[64:79]
	ds_read_b128 v[168:171], v192 offset:10240
	v_exp_f32_e32 v202, v34
	v_add_f32_e32 v201, 1.0, v201
	v_mfma_f32_32x32x16_f16 v[80:95], a[4:7], v[172:175], v[80:95]
	ds_read_b128 v[172:175], v192 offset:11264
	global_load_lds_dwordx4 v192, s[44:45] offset:1024 sc1
	v_exp_f32_e32 v203, v35
	v_add_f32_e32 v202, 1.0, v202
	s_waitcnt lgkmcnt(4)
	v_mfma_f32_32x32x16_f16 v[64:79], a[8:11], v[176:179], v[64:79]
	ds_read_b128 v[176:179], v192 offset:12288
	v_exp_f32_e32 v204, v36
	v_add_f32_e32 v203, 1.0, v203
	v_mfma_f32_32x32x16_f16 v[80:95], a[8:11], v[180:183], v[80:95]
	ds_read_b128 v[180:183], v192 offset:13312
	v_exp_f32_e32 v205, v37
	v_add_f32_e32 v204, 1.0, v204
	v_mfma_f32_32x32x16_f16 v[64:79], a[12:15], v[184:187], v[64:79]
	ds_read_b128 v[184:187], v192 offset:14336
	v_exp_f32_e32 v206, v38
	v_add_f32_e32 v205, 1.0, v205
	v_mfma_f32_32x32x16_f16 v[80:95], a[12:15], v[188:191], v[80:95]
	ds_read_b128 v[188:191], v192 offset:15360
	global_load_lds_dwordx4 v192, s[44:45] offset:2048 sc1
	v_exp_f32_e32 v207, v39
	v_add_f32_e32 v206, 1.0, v206
	s_waitcnt lgkmcnt(4)
	v_mfma_f32_32x32x16_f16 v[64:79], a[16:19], v[160:163], v[64:79]
	ds_read_b128 v[160:163], v192 offset:16384
	v_exp_f32_e32 v208, v40
	v_add_f32_e32 v207, 1.0, v207
	v_mfma_f32_32x32x16_f16 v[80:95], a[16:19], v[164:167], v[80:95]
	ds_read_b128 v[164:167], v192 offset:17408
	v_exp_f32_e32 v209, v41
	v_add_f32_e32 v208, 1.0, v208
	v_mfma_f32_32x32x16_f16 v[64:79], a[20:23], v[168:171], v[64:79]
	ds_read_b128 v[168:171], v192 offset:18432
	v_exp_f32_e32 v210, v42
	v_add_f32_e32 v209, 1.0, v209
	v_mfma_f32_32x32x16_f16 v[80:95], a[20:23], v[172:175], v[80:95]
	ds_read_b128 v[172:175], v192 offset:19456
	global_load_lds_dwordx4 v192, s[44:45] offset:3072 sc1
	v_exp_f32_e32 v211, v43
	v_add_f32_e32 v210, 1.0, v210
	s_waitcnt lgkmcnt(4)
	v_mfma_f32_32x32x16_f16 v[64:79], a[24:27], v[176:179], v[64:79]
	ds_read_b128 v[176:179], v192 offset:20480
	v_exp_f32_e32 v212, v44
	v_add_f32_e32 v211, 1.0, v211
	v_mfma_f32_32x32x16_f16 v[80:95], a[24:27], v[180:183], v[80:95]
	ds_read_b128 v[180:183], v192 offset:21504
	v_exp_f32_e32 v213, v45
	v_add_f32_e32 v212, 1.0, v212
	v_mfma_f32_32x32x16_f16 v[64:79], a[28:31], v[184:187], v[64:79]
	ds_read_b128 v[184:187], v192 offset:22528
	v_exp_f32_e32 v214, v46
	v_add_f32_e32 v213, 1.0, v213
	v_mfma_f32_32x32x16_f16 v[80:95], a[28:31], v[188:191], v[80:95]
	ds_read_b128 v[188:191], v192 offset:23552
	s_add_u32 s44, s34, 0x11000
	s_addc_u32 s45, s35, 0
	s_mov_b32 m0, s57
	s_nop 0
	global_load_lds_dwordx4 v192, s[44:45] sc1
	v_exp_f32_e32 v215, v47
	v_add_f32_e32 v214, 1.0, v214
	s_waitcnt lgkmcnt(4)
	v_mfma_f32_32x32x16_f16 v[64:79], a[32:35], v[160:163], v[64:79]
	ds_read_b128 v[160:163], v192 offset:24576
	v_add_f32_e32 v215, 1.0, v215
	v_rcp_f32_e32 v200, v200
	v_mfma_f32_32x32x16_f16 v[80:95], a[32:35], v[164:167], v[80:95]
	ds_read_b128 v[164:167], v192 offset:25600
	v_rcp_f32_e32 v201, v201
	v_mfma_f32_32x32x16_f16 v[64:79], a[36:39], v[168:171], v[64:79]
	ds_read_b128 v[168:171], v192 offset:26624
	v_rcp_f32_e32 v202, v202
	v_mfma_f32_32x32x16_f16 v[80:95], a[36:39], v[172:175], v[80:95]
	ds_read_b128 v[172:175], v192 offset:27648
	global_load_lds_dwordx4 v192, s[44:45] offset:1024 sc1
	v_rcp_f32_e32 v203, v203
	s_waitcnt lgkmcnt(4)
	v_mfma_f32_32x32x16_f16 v[64:79], a[40:43], v[176:179], v[64:79]
	ds_read_b128 v[176:179], v192 offset:28672
	v_rcp_f32_e32 v204, v204
	v_mfma_f32_32x32x16_f16 v[80:95], a[40:43], v[180:183], v[80:95]
	ds_read_b128 v[180:183], v192 offset:29696
	v_rcp_f32_e32 v205, v205
	v_mul_f32_e32 v204, v204, v136
	v_mfma_f32_32x32x16_f16 v[64:79], a[44:47], v[184:187], v[64:79]
	ds_read_b128 v[184:187], v192 offset:30720
	v_rcp_f32_e32 v206, v206
	v_mul_f32_e32 v205, v205, v137
	v_mfma_f32_32x32x16_f16 v[80:95], a[44:47], v[188:191], v[80:95]
	ds_read_b128 v[188:191], v192 offset:31744
	global_load_lds_dwordx4 v192, s[44:45] offset:2048 sc1
	v_rcp_f32_e32 v207, v207
	v_mul_f32_e32 v206, v206, v138
	s_waitcnt vmcnt(10)
	s_barrier
	s_waitcnt lgkmcnt(4)
	v_mfma_f32_32x32x16_f16 v[64:79], a[48:51], v[160:163], v[64:79]
	ds_read_b128 v[160:163], v192 offset:32768
	v_rcp_f32_e32 v208, v208
	v_mul_f32_e32 v207, v207, v139
	v_mfma_f32_32x32x16_f16 v[80:95], a[48:51], v[164:167], v[80:95]
	ds_read_b128 v[164:167], v192 offset:33792
	v_rcp_f32_e32 v209, v209
	v_fmamk_f32 v208, v208, 0xc0b8aa3b, v198
	v_mfma_f32_32x32x16_f16 v[64:79], a[52:55], v[168:171], v[64:79]
	ds_read_b128 v[168:171], v192 offset:34816
	v_rcp_f32_e32 v210, v210
	v_fmamk_f32 v209, v209, 0xc0b8aa3b, v198
	v_fma_f32 v136, v200, v208, v204
	v_mfma_f32_32x32x16_f16 v[80:95], a[52:55], v[172:175], v[80:95]
	ds_read_b128 v[172:175], v192 offset:35840
	global_load_lds_dwordx4 v192, s[44:45] offset:3072 sc1
	v_rcp_f32_e32 v211, v211
	v_fmamk_f32 v210, v210, 0xc0b8aa3b, v198
	v_fma_f32 v137, v201, v209, v205
	s_waitcnt lgkmcnt(4)
	v_mfma_f32_32x32x16_f16 v[64:79], a[56:59], v[176:179], v[64:79]
	ds_read_b128 v[176:179], v192 offset:36864
	v_rcp_f32_e32 v212, v212
	v_fmamk_f32 v211, v211, 0xc0b8aa3b, v198
	v_fma_f32 v138, v202, v210, v206
	v_mfma_f32_32x32x16_f16 v[80:95], a[56:59], v[180:183], v[80:95]
	ds_read_b128 v[180:183], v192 offset:37888
	v_rcp_f32_e32 v213, v213
	v_fma_f32 v139, v203, v211, v207
	v_mfma_f32_32x32x16_f16 v[64:79], a[60:63], v[184:187], v[64:79]
	ds_read_b128 v[184:187], v192 offset:38912
	v_rcp_f32_e32 v214, v214
	v_mfma_f32_32x32x16_f16 v[80:95], a[60:63], v[188:191], v[80:95]
	ds_read_b128 v[188:191], v192 offset:39936
	s_add_u32 s44, s34, 0x18000
	s_addc_u32 s45, s35, 0
	s_mov_b32 m0, s58
	s_nop 0
	global_load_lds_dwordx4 v192, s[44:45] sc1
	v_rcp_f32_e32 v215, v215
	s_waitcnt lgkmcnt(4)
	v_mfma_f32_32x32x16_f16 v[64:79], a[64:67], v[160:163], v[64:79]
	ds_read_b128 v[160:163], v192 offset:40960
	v_exp_f32_e32 v200, v136
	v_mfma_f32_32x32x16_f16 v[80:95], a[64:67], v[164:167], v[80:95]
	ds_read_b128 v[164:167], v192 offset:41984
	v_exp_f32_e32 v201, v137
	v_add_f32_e32 v200, 1.0, v200
	v_mfma_f32_32x32x16_f16 v[64:79], a[68:71], v[168:171], v[64:79]
	ds_read_b128 v[168:171], v192 offset:43008
	v_exp_f32_e32 v202, v138
	v_add_f32_e32 v201, 1.0, v201
	v_mfma_f32_32x32x16_f16 v[80:95], a[68:71], v[172:175], v[80:95]
	ds_read_b128 v[172:175], v192 offset:44032
	global_load_lds_dwordx4 v192, s[44:45] offset:1024 sc1
	v_exp_f32_e32 v203, v139
	v_add_f32_e32 v202, 1.0, v202
	s_waitcnt lgkmcnt(4)
	v_mfma_f32_32x32x16_f16 v[64:79], a[72:75], v[176:179], v[64:79]
	ds_read_b128 v[176:179], v192 offset:45056
	v_add_f32_e32 v203, 1.0, v203
	v_rcp_f32_e32 v200, v200
	v_mfma_f32_32x32x16_f16 v[80:95], a[72:75], v[180:183], v[80:95]
	ds_read_b128 v[180:183], v192 offset:46080
	v_rcp_f32_e32 v201, v201
	v_fma_f32 v200, v200, 2.0, -1.0
	v_mfma_f32_32x32x16_f16 v[64:79], a[76:79], v[184:187], v[64:79]
	ds_read_b128 v[184:187], v192 offset:47104
	v_rcp_f32_e32 v202, v202
	v_fma_f32 v201, v201, 2.0, -1.0
	v_mul_f32_e32 v216, v212, v200
	v_mfma_f32_32x32x16_f16 v[80:95], a[76:79], v[188:191], v[80:95]
	ds_read_b128 v[188:191], v192 offset:48128
	global_load_lds_dwordx4 v192, s[44:45] offset:2048 sc1
	v_rcp_f32_e32 v203, v203
	v_fma_f32 v202, v202, 2.0, -1.0
	v_mul_f32_e32 v217, v213, v201
	s_waitcnt lgkmcnt(4)
	v_mfma_f32_32x32x16_f16 v[64:79], a[80:83], v[160:163], v[64:79]
	ds_read_b128 v[160:163], v192 offset:49152
	v_fma_f32 v203, v203, 2.0, -1.0
	v_mul_f32_e32 v218, v214, v202
	v_exp_f32_e32 v200, v48
	v_mfma_f32_32x32x16_f16 v[80:95], a[80:83], v[164:167], v[80:95]
	ds_read_b128 v[164:167], v192 offset:50176
	v_mul_f32_e32 v219, v215, v203
	v_cvt_pk_f16_f32 v220, v216, v217
	v_exp_f32_e32 v201, v49
	v_mfma_f32_32x32x16_f16 v[64:79], a[84:87], v[168:171], v[64:79]
	ds_read_b128 v[168:171], v192 offset:51200
	v_cvt_pk_f16_f32 v221, v218, v219
	v_exp_f32_e32 v202, v50
	v_add_f32_e32 v200, 1.0, v200
	v_mfma_f32_32x32x16_f16 v[80:95], a[84:87], v[172:175], v[80:95]
	ds_read_b128 v[172:175], v192 offset:52224
	global_load_lds_dwordx4 v192, s[44:45] offset:3072 sc1
	s_cmp_lg_u32 s33, s60
	s_cbranch_scc1 .LE_nht34
	s_add_u32 s46, s62, 0x40000
	s_addc_u32 s47, s63, 0
	global_store_dwordx4 v250, v[216:219], s[46:47]
	s_waitcnt vmcnt(0)

.LE_join41:
	v_mfma_f32_32x32x16_f16 v[64:79], a[196:199], v[168:171], v[64:79]
	ds_read_b128 v[168:171], v193 offset:43008
	v_mfma_f32_32x32x16_f16 v[80:95], a[196:199], v[172:175], v[80:95]
	ds_read_b128 v[172:175], v193 offset:44032
	global_load_lds_dwordx4 v192, s[44:45] offset:1024 sc1
	s_waitcnt lgkmcnt(4)
	v_mfma_f32_32x32x16_f16 v[64:79], a[200:203], v[176:179], v[64:79]
	ds_read_b128 v[176:179], v193 offset:45056
	v_mfma_f32_32x32x16_f16 v[80:95], a[200:203], v[180:183], v[80:95]
	ds_read_b128 v[180:183], v193 offset:46080
	s_and_b32 s64, s33, 1
	s_lshl_b32 s64, s64, 22
	s_add_u32 s64, s64, s50
	s_add_u32 s64, s64, 0x40000
	s_add_u32 s36, s6, s64
	s_addc_u32 s37, s7, 0
	s_lshl_b32 s64, s33, 3
	s_add_u32 s64, s64, s29
	s_lshl_b32 s64, s64, 5
	s_add_u32 s64, s64, s30
	s_lshl_b32 s64, s64, 2
	s_add_u32 s40, s8, s64
	s_addc_u32 s41, s9, 0
	s_lshl_b32 s64, s61, 11
	s_lshl_b32 s65, s29, 8
	s_add_u32 s64, s64, s65
	s_add_u32 s64, s64, 64
	s_lshl_b32 s64, s64, 3
	s_add_u32 s42, s12, s64
	s_addc_u32 s43, s13, 0
	v_mfma_f32_32x32x16_f16 v[64:79], a[204:207], v[184:187], v[64:79]
	ds_read_b128 v[184:187], v193 offset:47104
	v_mfma_f32_32x32x16_f16 v[80:95], a[204:207], v[188:191], v[80:95]
	ds_read_b128 v[188:191], v193 offset:48128
	global_load_lds_dwordx4 v192, s[44:45] offset:2048 sc1
	s_waitcnt lgkmcnt(4)
	v_mfma_f32_32x32x16_f16 v[64:79], a[208:211], v[160:163], v[64:79]
	ds_read_b128 v[160:163], v193 offset:49152
	v_mfma_f32_32x32x16_f16 v[80:95], a[208:211], v[164:167], v[80:95]
	ds_read_b128 v[164:167], v193 offset:50176
	v_mfma_f32_32x32x16_f16 v[64:79], a[212:215], v[168:171], v[64:79]
	ds_read_b128 v[168:171], v193 offset:51200
	v_mfma_f32_32x32x16_f16 v[80:95], a[212:215], v[172:175], v[80:95]
	ds_read_b128 v[172:175], v193 offset:52224
	global_load_lds_dwordx4 v192, s[44:45] offset:3072 sc1
	s_waitcnt lgkmcnt(4)
	v_mfma_f32_32x32x16_f16 v[64:79], a[216:219], v[176:179], v[64:79]
	ds_read_b128 v[176:179], v193 offset:53248
	v_mfma_f32_32x32x16_f16 v[80:95], a[216:219], v[180:183], v[80:95]
	ds_read_b128 v[180:183], v193 offset:54272
	v_mfma_f32_32x32x16_f16 v[64:79], a[220:223], v[184:187], v[64:79]
	ds_read_b128 v[184:187], v193 offset:55296
	v_mfma_f32_32x32x16_f16 v[80:95], a[220:223], v[188:191], v[80:95]
	ds_read_b128 v[188:191], v193 offset:56320
	s_add_u32 s44, s34, 0x9000
	s_addc_u32 s45, s35, 0
	s_mov_b32 m0, s55
	s_nop 0
	global_load_lds_dwordx4 v192, s[44:45] sc1
	s_waitcnt lgkmcnt(4)
	v_mfma_f32_32x32x16_f16 v[64:79], a[224:227], v[160:163], v[64:79]
	ds_read_b128 v[160:163], v193 offset:57344
	v_mfma_f32_32x32x16_f16 v[80:95], a[224:227], v[164:167], v[80:95]
	ds_read_b128 v[164:167], v193 offset:58368
	v_mfma_f32_32x32x16_f16 v[64:79], a[228:231], v[168:171], v[64:79]
	ds_read_b128 v[168:171], v193 offset:59392
	v_mfma_f32_32x32x16_f16 v[80:95], a[228:231], v[172:175], v[80:95]
	ds_read_b128 v[172:175], v193 offset:60416
	global_load_lds_dwordx4 v192, s[44:45] offset:1024 sc1
	s_waitcnt lgkmcnt(4)
	v_mfma_f32_32x32x16_f16 v[64:79], a[232:235], v[176:179], v[64:79]
	ds_read_b128 v[176:179], v193 offset:61440
	v_mfma_f32_32x32x16_f16 v[80:95], a[232:235], v[180:183], v[80:95]
	ds_read_b128 v[180:183], v193 offset:62464
	v_mfma_f32_32x32x16_f16 v[64:79], a[236:239], v[184:187], v[64:79]
	ds_read_b128 v[184:187], v193 offset:63488
	v_mfma_f32_32x32x16_f16 v[80:95], a[236:239], v[188:191], v[80:95]
	ds_read_b128 v[188:191], v193 offset:64512
	global_load_lds_dwordx4 v192, s[44:45] offset:2048 sc1
	s_waitcnt vmcnt(8)
	s_barrier
	s_waitcnt lgkmcnt(4)
	v_mfma_f32_32x32x16_f16 v[64:79], a[240:243], v[160:163], v[64:79]
	ds_read_b128 v[160:163], v192 offset:0
	v_mfma_f32_32x32x16_f16 v[80:95], a[240:243], v[164:167], v[80:95]
	ds_read_b128 v[164:167], v192 offset:1024
	v_mfma_f32_32x32x16_f16 v[64:79], a[244:247], v[168:171], v[64:79]
	ds_read_b128 v[168:171], v192 offset:2048
	v_mfma_f32_32x32x16_f16 v[80:95], a[244:247], v[172:175], v[80:95]
	ds_read_b128 v[172:175], v192 offset:3072
	global_load_lds_dwordx4 v192, s[44:45] offset:3072 sc1
	s_waitcnt lgkmcnt(4)
	v_mfma_f32_32x32x16_f16 v[64:79], a[248:251], v[176:179], v[64:79]
	ds_read_b128 v[176:179], v192 offset:4096
	v_mfma_f32_32x32x16_f16 v[80:95], a[248:251], v[180:183], v[80:95]
	ds_read_b128 v[180:183], v192 offset:5120
	v_mfma_f32_32x32x16_f16 v[64:79], a[252:255], v[184:187], v[64:79]
	ds_read_b128 v[184:187], v192 offset:6144
	v_mfma_f32_32x32x16_f16 v[80:95], a[252:255], v[188:191], v[80:95]
	ds_read_b128 v[188:191], v192 offset:7168
	s_add_u32 s44, s34, 0x10000
	s_addc_u32 s45, s35, 0
	s_mov_b32 m0, s56
	s_nop 0
	global_load_lds_dwordx4 v192, s[44:45] sc1
	s_nop 3
	global_load_dword v228, v249, s[42:43] offset:0
	global_load_dword v229, v249, s[42:43] offset:256
	s_waitcnt lgkmcnt(4)
	v_mfma_f32_32x32x16_f16 v[96:111], a[0:3], v[160:163], v[96:111]
	ds_read_b128 v[160:163], v192 offset:8192
	v_exp_f32_e32 v200, v64
	v_mfma_f32_32x32x16_f16 v[112:127], a[0:3], v[164:167], v[112:127]
	ds_read_b128 v[164:167], v192 offset:9216
	s_lshl_b32 s64, s33, 3
	s_add_u32 s64, s64, s29
	s_lshl_b32 s64, s64, 7
	s_add_u32 s38, s8, s64
	s_addc_u32 s39, s9, 0
	global_load_dword v251, v196, s[38:39] sc1
	v_exp_f32_e32 v201, v65
	v_add_f32_e32 v200, 1.0, v200
	v_mfma_f32_32x32x16_f16 v[96:111], a[4:7], v[168:171], v[96:111]
	ds_read_b128 v[168:171], v192 offset:10240
	v_exp_f32_e32 v202, v66
	v_add_f32_e32 v201, 1.0, v201
	v_mfma_f32_32x32x16_f16 v[112:127], a[4:7], v[172:175], v[112:127]
	ds_read_b128 v[172:175], v192 offset:11264
	global_load_lds_dwordx4 v192, s[44:45] offset:1024 sc1
	v_exp_f32_e32 v203, v67
	v_add_f32_e32 v202, 1.0, v202
	s_waitcnt lgkmcnt(4)
	v_mfma_f32_32x32x16_f16 v[96:111], a[8:11], v[176:179], v[96:111]
	ds_read_b128 v[176:179], v192 offset:12288
	v_exp_f32_e32 v204, v68
	v_add_f32_e32 v203, 1.0, v203
	v_mfma_f32_32x32x16_f16 v[112:127], a[8:11], v[180:183], v[112:127]
	ds_read_b128 v[180:183], v192 offset:13312
	v_exp_f32_e32 v205, v69
	v_add_f32_e32 v204, 1.0, v204
	v_mfma_f32_32x32x16_f16 v[96:111], a[12:15], v[184:187], v[96:111]
	ds_read_b128 v[184:187], v192 offset:14336
	v_exp_f32_e32 v206, v70
	v_add_f32_e32 v205, 1.0, v205
	v_mfma_f32_32x32x16_f16 v[112:127], a[12:15], v[188:191], v[112:127]
	ds_read_b128 v[188:191], v192 offset:15360
	global_load_lds_dwordx4 v192, s[44:45] offset:2048 sc1
	v_exp_f32_e32 v207, v71
	v_add_f32_e32 v206, 1.0, v206
	s_waitcnt lgkmcnt(4)
	v_mfma_f32_32x32x16_f16 v[96:111], a[16:19], v[160:163], v[96:111]
	ds_read_b128 v[160:163], v192 offset:16384
	v_exp_f32_e32 v208, v72
	v_add_f32_e32 v207, 1.0, v207
	v_mfma_f32_32x32x16_f16 v[112:127], a[16:19], v[164:167], v[112:127]
	ds_read_b128 v[164:167], v192 offset:17408
	v_exp_f32_e32 v209, v73
	v_add_f32_e32 v208, 1.0, v208
	v_mfma_f32_32x32x16_f16 v[96:111], a[20:23], v[168:171], v[96:111]
	ds_read_b128 v[168:171], v192 offset:18432
	v_exp_f32_e32 v210, v74
	v_add_f32_e32 v209, 1.0, v209
	v_mfma_f32_32x32x16_f16 v[112:127], a[20:23], v[172:175], v[112:127]
	ds_read_b128 v[172:175], v192 offset:19456
	global_load_lds_dwordx4 v192, s[44:45] offset:3072 sc1
	v_exp_f32_e32 v211, v75
	v_add_f32_e32 v210, 1.0, v210
	s_waitcnt lgkmcnt(4)
	v_mfma_f32_32x32x16_f16 v[96:111], a[24:27], v[176:179], v[96:111]
	ds_read_b128 v[176:179], v192 offset:20480
	v_exp_f32_e32 v212, v76
	v_add_f32_e32 v211, 1.0, v211
	v_mfma_f32_32x32x16_f16 v[112:127], a[24:27], v[180:183], v[112:127]
	ds_read_b128 v[180:183], v192 offset:21504
	v_exp_f32_e32 v213, v77
	v_add_f32_e32 v212, 1.0, v212
	v_mfma_f32_32x32x16_f16 v[96:111], a[28:31], v[184:187], v[96:111]
	ds_read_b128 v[184:187], v192 offset:22528
	v_exp_f32_e32 v214, v78
	v_add_f32_e32 v213, 1.0, v213
	v_mfma_f32_32x32x16_f16 v[112:127], a[28:31], v[188:191], v[112:127]
	ds_read_b128 v[188:191], v192 offset:23552
	s_add_u32 s44, s34, 0x11000
	s_addc_u32 s45, s35, 0
	s_mov_b32 m0, s57
	s_nop 0
	global_load_lds_dwordx4 v192, s[44:45] sc1
	v_exp_f32_e32 v215, v79
	v_add_f32_e32 v214, 1.0, v214
	s_waitcnt lgkmcnt(4)
	v_mfma_f32_32x32x16_f16 v[96:111], a[32:35], v[160:163], v[96:111]
	ds_read_b128 v[160:163], v192 offset:24576
	v_add_f32_e32 v215, 1.0, v215
	v_rcp_f32_e32 v200, v200
	v_mfma_f32_32x32x16_f16 v[112:127], a[32:35], v[164:167], v[112:127]
	ds_read_b128 v[164:167], v192 offset:25600
	v_rcp_f32_e32 v201, v201
	v_mfma_f32_32x32x16_f16 v[96:111], a[36:39], v[168:171], v[96:111]
	ds_read_b128 v[168:171], v192 offset:26624
	v_rcp_f32_e32 v202, v202
	v_mfma_f32_32x32x16_f16 v[112:127], a[36:39], v[172:175], v[112:127]
	ds_read_b128 v[172:175], v192 offset:27648
	global_load_lds_dwordx4 v192, s[44:45] offset:1024 sc1
	v_rcp_f32_e32 v203, v203
	s_waitcnt lgkmcnt(4)
	v_mfma_f32_32x32x16_f16 v[96:111], a[40:43], v[176:179], v[96:111]
	ds_read_b128 v[176:179], v192 offset:28672
	v_rcp_f32_e32 v204, v204
	v_mfma_f32_32x32x16_f16 v[112:127], a[40:43], v[180:183], v[112:127]
	ds_read_b128 v[180:183], v192 offset:29696
	v_rcp_f32_e32 v205, v205
	v_mul_f32_e32 v204, v204, v144
	v_mfma_f32_32x32x16_f16 v[96:111], a[44:47], v[184:187], v[96:111]
	ds_read_b128 v[184:187], v192 offset:30720
	v_rcp_f32_e32 v206, v206
	v_mul_f32_e32 v205, v205, v145
	v_mfma_f32_32x32x16_f16 v[112:127], a[44:47], v[188:191], v[112:127]
	ds_read_b128 v[188:191], v192 offset:31744
	global_load_lds_dwordx4 v192, s[44:45] offset:2048 sc1
	v_rcp_f32_e32 v207, v207
	v_mul_f32_e32 v206, v206, v146
	s_waitcnt vmcnt(10)
	s_barrier
	s_waitcnt lgkmcnt(4)
	v_mfma_f32_32x32x16_f16 v[96:111], a[48:51], v[160:163], v[96:111]
	ds_read_b128 v[160:163], v192 offset:32768
	v_rcp_f32_e32 v208, v208
	v_mul_f32_e32 v207, v207, v147
	v_mfma_f32_32x32x16_f16 v[112:127], a[48:51], v[164:167], v[112:127]
	ds_read_b128 v[164:167], v192 offset:33792
	v_rcp_f32_e32 v209, v209
	v_fmamk_f32 v208, v208, 0xc0b8aa3b, v198
	v_mfma_f32_32x32x16_f16 v[96:111], a[52:55], v[168:171], v[96:111]
	ds_read_b128 v[168:171], v192 offset:34816
	v_rcp_f32_e32 v210, v210
	v_fmamk_f32 v209, v209, 0xc0b8aa3b, v198
	v_fma_f32 v144, v200, v208, v204
	v_mfma_f32_32x32x16_f16 v[112:127], a[52:55], v[172:175], v[112:127]
	ds_read_b128 v[172:175], v192 offset:35840
	global_load_lds_dwordx4 v192, s[44:45] offset:3072 sc1
	v_rcp_f32_e32 v211, v211
	v_fmamk_f32 v210, v210, 0xc0b8aa3b, v198
	v_fma_f32 v145, v201, v209, v205
	s_waitcnt lgkmcnt(4)
	v_mfma_f32_32x32x16_f16 v[96:111], a[56:59], v[176:179], v[96:111]
	ds_read_b128 v[176:179], v192 offset:36864
	v_rcp_f32_e32 v212, v212
	v_fmamk_f32 v211, v211, 0xc0b8aa3b, v198
	v_fma_f32 v146, v202, v210, v206
	v_mfma_f32_32x32x16_f16 v[112:127], a[56:59], v[180:183], v[112:127]
	ds_read_b128 v[180:183], v192 offset:37888
	v_rcp_f32_e32 v213, v213
	v_fma_f32 v147, v203, v211, v207
	v_mfma_f32_32x32x16_f16 v[96:111], a[60:63], v[184:187], v[96:111]
	ds_read_b128 v[184:187], v192 offset:38912
	v_rcp_f32_e32 v214, v214
	v_mfma_f32_32x32x16_f16 v[112:127], a[60:63], v[188:191], v[112:127]
	ds_read_b128 v[188:191], v192 offset:39936
	s_add_u32 s44, s34, 0x18000
	s_addc_u32 s45, s35, 0
	s_mov_b32 m0, s58
	s_nop 0
	global_load_lds_dwordx4 v192, s[44:45] sc1
	v_rcp_f32_e32 v215, v215
	s_waitcnt lgkmcnt(4)
	v_mfma_f32_32x32x16_f16 v[96:111], a[64:67], v[160:163], v[96:111]
	ds_read_b128 v[160:163], v192 offset:40960
	v_exp_f32_e32 v200, v144
	v_mfma_f32_32x32x16_f16 v[112:127], a[64:67], v[164:167], v[112:127]
	ds_read_b128 v[164:167], v192 offset:41984
	v_exp_f32_e32 v201, v145
	v_add_f32_e32 v200, 1.0, v200
	v_mfma_f32_32x32x16_f16 v[96:111], a[68:71], v[168:171], v[96:111]
	ds_read_b128 v[168:171], v192 offset:43008
	v_exp_f32_e32 v202, v146
	v_add_f32_e32 v201, 1.0, v201
	v_mfma_f32_32x32x16_f16 v[112:127], a[68:71], v[172:175], v[112:127]
	ds_read_b128 v[172:175], v192 offset:44032
	global_load_lds_dwordx4 v192, s[44:45] offset:1024 sc1
	v_exp_f32_e32 v203, v147
	v_add_f32_e32 v202, 1.0, v202
	s_waitcnt lgkmcnt(4)
	v_mfma_f32_32x32x16_f16 v[96:111], a[72:75], v[176:179], v[96:111]
	ds_read_b128 v[176:179], v192 offset:45056
	v_add_f32_e32 v203, 1.0, v203
	v_rcp_f32_e32 v200, v200
	v_mfma_f32_32x32x16_f16 v[112:127], a[72:75], v[180:183], v[112:127]
	ds_read_b128 v[180:183], v192 offset:46080
	v_rcp_f32_e32 v201, v201
	v_fma_f32 v200, v200, 2.0, -1.0
	v_mfma_f32_32x32x16_f16 v[96:111], a[76:79], v[184:187], v[96:111]
	ds_read_b128 v[184:187], v192 offset:47104
	v_rcp_f32_e32 v202, v202
	v_fma_f32 v201, v201, 2.0, -1.0
	v_mul_f32_e32 v216, v212, v200
	v_mfma_f32_32x32x16_f16 v[112:127], a[76:79], v[188:191], v[112:127]
	ds_read_b128 v[188:191], v192 offset:48128
	global_load_lds_dwordx4 v192, s[44:45] offset:2048 sc1
	v_rcp_f32_e32 v203, v203
	v_fma_f32 v202, v202, 2.0, -1.0
	v_mul_f32_e32 v217, v213, v201
	s_waitcnt lgkmcnt(4)
	v_mfma_f32_32x32x16_f16 v[96:111], a[80:83], v[160:163], v[96:111]
	ds_read_b128 v[160:163], v192 offset:49152
	v_fma_f32 v203, v203, 2.0, -1.0
	v_mul_f32_e32 v218, v214, v202
	v_exp_f32_e32 v200, v80
	v_mfma_f32_32x32x16_f16 v[112:127], a[80:83], v[164:167], v[112:127]
	ds_read_b128 v[164:167], v192 offset:50176
	v_mul_f32_e32 v219, v215, v203
	v_cvt_pk_f16_f32 v220, v216, v217
	v_exp_f32_e32 v201, v81
	v_mfma_f32_32x32x16_f16 v[96:111], a[84:87], v[168:171], v[96:111]
	ds_read_b128 v[168:171], v192 offset:51200
	v_cvt_pk_f16_f32 v221, v218, v219
	v_exp_f32_e32 v202, v82
	v_add_f32_e32 v200, 1.0, v200
	v_mfma_f32_32x32x16_f16 v[112:127], a[84:87], v[172:175], v[112:127]
	ds_read_b128 v[172:175], v192 offset:52224
	global_load_lds_dwordx4 v192, s[44:45] offset:3072 sc1
	s_cmp_lg_u32 s33, s60
	s_cbranch_scc1 .LE_nht42
	s_add_u32 s46, s62, 0x80000
	s_addc_u32 s47, s63, 0
	global_store_dwordx4 v250, v[216:219], s[46:47]
	s_waitcnt vmcnt(0)
